# speedup vs baseline: 1.0064x; 1.0064x over previous
.Lfc_step:
	v_mfma_f32_32x32x16_f16 v[0:15], v[120:123], v[32:35], 0
	v_mfma_f32_32x32x16_f16 v[16:31], v[120:123], v[60:63], 0
	v_mfma_f32_32x32x16_f16 v[0:15], v[124:127], v[36:39], v[0:15]
	v_mfma_f32_32x32x16_f16 v[16:31], v[124:127], v[64:67], v[16:31]
	v_mfma_f32_32x32x16_f16 v[0:15], v[128:131], v[40:43], v[0:15]
	v_mfma_f32_32x32x16_f16 v[16:31], v[128:131], v[68:71], v[16:31]
	v_mfma_f32_32x32x16_f16 v[0:15], v[132:135], v[44:47], v[0:15]
	v_mfma_f32_32x32x16_f16 v[16:31], v[132:135], v[72:75], v[16:31]
	v_mfma_f32_32x32x16_f16 v[0:15], v[136:139], v[48:51], v[0:15]
	v_mfma_f32_32x32x16_f16 v[16:31], v[136:139], v[76:79], v[16:31]
	v_mfma_f32_32x32x16_f16 v[0:15], v[140:143], v[52:55], v[0:15]
	v_mfma_f32_32x32x16_f16 v[16:31], v[140:143], v[80:83], v[16:31]
	v_mfma_f32_32x32x16_f16 v[0:15], v[144:147], v[56:59], v[0:15]
	v_mfma_f32_32x32x16_f16 v[16:31], v[144:147], v[84:87], v[16:31]
	s_nop 11
	s_barrier
	ds_write_b32 v102, v0 offset:0
	ds_write_b32 v102, v1 offset:1024
	ds_write_b32 v102, v2 offset:2048
	ds_write_b32 v102, v3 offset:3072
	ds_write_b32 v102, v4 offset:8192
	ds_write_b32 v102, v5 offset:9216
	ds_write_b32 v102, v6 offset:10240
	ds_write_b32 v102, v7 offset:11264
	ds_write_b32 v102, v8 offset:16384
	ds_write_b32 v102, v9 offset:17408
	ds_write_b32 v102, v10 offset:18432
	ds_write_b32 v102, v11 offset:19456
	ds_write_b32 v102, v12 offset:24576
	ds_write_b32 v102, v13 offset:25600
	ds_write_b32 v102, v14 offset:26624
	ds_write_b32 v102, v15 offset:27648
	ds_write_b32 v102, v16 offset:128
	ds_write_b32 v102, v17 offset:1152
	ds_write_b32 v102, v18 offset:2176
	ds_write_b32 v102, v19 offset:3200
	ds_write_b32 v102, v20 offset:8320
	ds_write_b32 v102, v21 offset:9344
	ds_write_b32 v102, v22 offset:10368
	ds_write_b32 v102, v23 offset:11392
	ds_write_b32 v102, v24 offset:16512
	ds_write_b32 v102, v25 offset:17536
	ds_write_b32 v102, v26 offset:18560
	ds_write_b32 v102, v27 offset:19584
	ds_write_b32 v102, v28 offset:24704
	ds_write_b32 v102, v29 offset:25728
	ds_write_b32 v102, v30 offset:26752
	ds_write_b32 v102, v31 offset:27776
	s_waitcnt lgkmcnt(0)
	s_barrier
	ds_read_b128 v[120:123], v88
	ds_read_b128 v[124:127], v88 offset:1024
	ds_read_b128 v[128:131], v88 offset:2048
	ds_read_b128 v[132:135], v88 offset:3072
	ds_read_b128 v[136:139], v88 offset:4096
	ds_read_b128 v[140:143], v88 offset:5120
	ds_read_b128 v[144:147], v88 offset:6144
	v_add_u32_e32 v88, 0x1c00, v88
	ds_read_b128 v[0:3], v103
	ds_read_b128 v[4:7], v103 offset:1024
	ds_read_b128 v[8:11], v103 offset:2048
	ds_read_b128 v[12:15], v103 offset:3072
	ds_read_b128 v[16:19], v103 offset:4096
	ds_read_b128 v[20:23], v103 offset:5120
	ds_read_b128 v[24:27], v103 offset:6144
	ds_read_b128 v[28:31], v103 offset:7168
	s_mov_b64 exec, s[24:25]
	s_waitcnt lgkmcnt(7)
	global_store_dwordx4 v104, v[0:3], s[8:9] nt
	s_waitcnt lgkmcnt(6)
	global_store_dwordx4 v105, v[4:7], s[8:9] nt
	s_waitcnt lgkmcnt(5)
	global_store_dwordx4 v106, v[8:11], s[8:9] nt
	s_waitcnt lgkmcnt(4)
	global_store_dwordx4 v107, v[12:15], s[8:9] nt
	s_waitcnt lgkmcnt(3)
	global_store_dwordx4 v108, v[16:19], s[8:9] nt
	s_waitcnt lgkmcnt(2)
	global_store_dwordx4 v109, v[20:23], s[8:9] nt
	s_waitcnt lgkmcnt(1)
	global_store_dwordx4 v110, v[24:27], s[8:9] nt
	s_waitcnt lgkmcnt(0)
	global_store_dwordx4 v111, v[28:31], s[8:9] nt
	s_mov_b64 exec, -1
	s_waitcnt vmcnt(8)
	s_add_u32 s8, s8, 0x61a800
	s_addc_u32 s9, s9, 0
	s_add_i32 s0, s0, 1
	s_cmp_lt_u32 s0, 8
	s_cbranch_scc1 .Lfc_step
	s_cmp_eq_u32 s20, 15
	s_cbranch_scc1 .Lfc_exit
	s_add_i32 s20, s20, 1
	s_branch .Lfc_seg
